# T5: s_setprio flips additionally around the spatial-gating unit's four MFMA groups
# baseline (speedup 1.0000x reference)
; __device__ __forceinline__ int crow(int r, int hi) { return (r & 3) + 8 * (r >> 2) + 4 * hi; }
; __device__ __forceinline__ void unit(const bf16_t* proj, const float* stats  , const float* lng, const float* lnb, const float* sw, const float* sb, bf16_t* Y2, int un, LAS unsigned char* lds) {
;     int tid_l = threadIdx.x; asm volatile("" : "+v"(tid_l));
;     const int tid = tid_l, wid = __builtin_amdgcn_readfirstlane(tid >> 6), lane = tid & 63, r32 = lane & 31, hi = lane >> 5;
;     const int g = un & 7, R0 = (un >> 3) * 128;
;     const int tb = wid & 3, eh = wid >> 2, t = tb * 32 + r32;
;     f32x4 wv[16]; unsigned uu[32], zq[32]; float bias[16];
; #pragma unroll
;     for (int i = 0; i < 8; ++i) { const int s0 = (i >> 2) * 64 + 16 * (i & 3) + hi * 8; const float* wp = sw + ((size_t)g * 128 + t) * 128 + s0; wv[2 * i] = *(const f32x4*)wp; wv[2 * i + 1] = *(const f32x4*)(wp + 4); }
; #pragma unroll
;     for (int r = 0; r < 16; ++r) { const int tr = tb * 32 + att::crow(r, hi), bt = R0 + tr; bias[r] = sb[g * 128 + tr];
; #pragma unroll
;         for (int d = 0; d < 2; ++d) { const int ch = g * 128 + (2 * eh + d) * 32 + (r32 & ~1); uu[r * 2 + d] = *(const unsigned*)(proj + (size_t)bt * NC + C_UC + ch); zq[r * 2 + d] = *(const unsigned*)(proj + (size_t)bt * NC + C_ZC + ch); } }
.LBB0_1376:
	s_andn2_b64 vcc, exec, s[0:1]
	s_cbranch_vccnz .LBB0_425
	v_readlane_b32 s4, v252, 35
	v_readlane_b32 s10, v252, 41
	v_readlane_b32 s11, v252, 42
	s_mov_b64 s[0:1], s[10:11]
	v_readlane_b32 s5, v252, 36
	v_readlane_b32 s12, v252, 43
	v_readlane_b32 s13, v252, 44
	v_readlane_b32 s10, v254, 43
	v_readlane_b32 s11, v254, 44
	s_add_u32 s0, s0, s10
	s_mov_b64 s[4:5], s[12:13]
	s_addc_u32 s1, s1, s11
	v_readlane_b32 s6, v252, 37
	v_readlane_b32 s7, v252, 38
	v_readlane_b32 s8, v252, 39
	v_readlane_b32 s9, v252, 40
	v_readlane_b32 s14, v252, 45
	v_readlane_b32 s15, v252, 46
	s_add_u32 s4, s4, s10
	s_addc_u32 s5, s5, s11
	s_mov_b64 s[6:7], s[14:15]
	v_readlane_b32 s8, v253, 54
	v_readlane_b32 s16, v252, 47
	v_readlane_b32 s17, v252, 48
	v_readlane_b32 s9, v253, 55
	s_add_u32 s12, s6, s8
	s_addc_u32 s13, s7, s9
	s_mov_b64 s[6:7], s[16:17]
	s_add_u32 s6, s6, s10
	v_readlane_b32 s8, v254, 47
	s_addc_u32 s7, s7, s11
	s_waitcnt vmcnt(23)
	v_mov_b32_e32 v176, v0
	s_and_b32 s2, s8, 7
	s_lshl_b32 s8, s8, 4
	s_add_i32 s8, s8, 0x7fffe000
	v_readfirstlane_b32 s10, v176
	s_and_b32 s11, s8, 0x7fffff80
	s_lshr_b32 s8, s10, 1
	v_and_b32_e32 v177, 31, v176
	s_and_b32 s9, s8, 0x60
	v_or_b32_e32 v182, s9, v177
	s_lshl_b32 s8, s2, 16
	s_waitcnt vmcnt(3)
	v_lshl_or_b32 v2, v182, 9, s8
	v_lshl_add_u64 v[4:5], s[12:13], 0, v[2:3]
	v_and_b32_e32 v2, 32, v176
	s_lshl_b32 s2, s2, 7
	s_ashr_i32 s8, s10, 2
	v_lshl_add_u64 v[40:41], v[4:5], 0, v[2:3]
	s_andn2_b32 s8, s8, 63
	v_and_or_b32 v2, v176, 30, s2
	s_waitcnt vmcnt(0)
	v_bfe_u32 v1, v176, 5, 1
	v_add_u32_e32 v68, s8, v2
	v_readlane_b32 s12, v253, 48
	v_lshlrev_b32_e32 v183, 3, v1
	v_lshl_or_b32 v1, v1, 2, s9
	v_ashrrev_i32_e32 v69, 31, v68
	v_readlane_b32 s13, v253, 49
	v_or_b32_e32 v2, s11, v1
	s_mov_b32 s14, 0xe800
	v_mov_b64_e32 v[100:101], s[12:13]
	v_lshlrev_b64 v[84:85], 1, v[68:69]
	v_or_b32_e32 v68, 32, v68
	v_readlane_b32 s18, v252, 49
	v_readlane_b32 s19, v252, 50
	v_mad_u64_u32 v[70:71], s[12:13], v2, s14, v[100:101]
	s_mov_b64 s[16:17], 0x4000
	v_ashrrev_i32_e32 v69, 31, v68
	v_lshl_add_u64 v[72:73], v[70:71], 0, s[16:17]
	s_mov_b64 s[18:19], 0x5000
	v_lshlrev_b64 v[86:87], 1, v[68:69]
	v_lshl_add_u64 v[70:71], v[70:71], 0, s[18:19]
	v_lshl_add_u64 v[74:75], v[72:73], 0, v[84:85]
	v_lshl_add_u64 v[68:69], v[72:73], 0, v[86:87]
	global_load_dwordx4 v[28:31], v[40:41], off offset:16
	global_load_dwordx4 v[32:35], v[40:41], off
	global_load_dwordx4 v[20:23], v[40:41], off offset:80
	global_load_dwordx4 v[24:27], v[40:41], off offset:64
	s_cmp_ge_u32 s9, 32
	s_cselect_b64 exec, -1, 0
	global_load_dwordx4 v[12:15], v[40:41], off offset:144
	global_load_dwordx4 v[16:19], v[40:41], off offset:128
	s_waitcnt lgkmcnt(0)
	global_load_dwordx4 v[4:7], v[40:41], off offset:208
	global_load_dwordx4 v[8:11], v[40:41], off offset:192
	s_cmp_ge_u32 s9, 64
	s_cselect_b64 exec, -1, 0
	global_load_dwordx4 v[60:63], v[40:41], off offset:272
	global_load_dwordx4 v[64:67], v[40:41], off offset:256
	global_load_dwordx4 v[52:55], v[40:41], off offset:336
	global_load_dwordx4 v[56:59], v[40:41], off offset:320
	s_cmp_ge_u32 s9, 0x60
	s_cselect_b64 exec, -1, 0
	global_load_dwordx4 v[44:47], v[40:41], off offset:400
	global_load_dwordx4 v[48:51], v[40:41], off offset:384
	global_load_dwordx4 v[36:39], v[40:41], off offset:464
	s_nop 0
	global_load_dwordx4 v[40:43], v[40:41], off offset:448
	s_mov_b64 exec, -1
	v_or_b32_e32 v1, s2, v1
	global_load_dword v180, v[74:75], off
	global_load_dword v178, v[68:69], off
	v_lshl_add_u64 v[74:75], v[70:71], 0, v[84:85]
	v_lshl_add_u64 v[68:69], v[70:71], 0, v[86:87]
	global_load_dword v181, v[74:75], off
	global_load_dword v179, v[68:69], off
	v_or_b32_e32 v68, 1, v2
	v_mad_u64_u32 v[68:69], s[12:13], v68, s14, v[100:101]
	v_lshl_add_u64 v[70:71], v[68:69], 0, s[16:17]
	v_lshl_add_u64 v[68:69], v[68:69], 0, s[18:19]
	v_lshl_add_u64 v[72:73], v[70:71], 0, v[84:85]
	v_lshl_add_u64 v[70:71], v[70:71], 0, v[86:87]
	global_load_dword v173, v[72:73], off
	global_load_dword v172, v[70:71], off
	v_lshl_add_u64 v[72:73], v[68:69], 0, v[84:85]
	v_lshl_add_u64 v[68:69], v[68:69], 0, v[86:87]
	global_load_dword v174, v[68:69], off
	v_or_b32_e32 v68, 2, v2
	v_mad_u64_u32 v[68:69], s[12:13], v68, s14, v[100:101]
	v_lshl_add_u64 v[70:71], v[68:69], 0, s[16:17]
	global_load_dword v175, v[72:73], off
	v_lshl_add_u64 v[68:69], v[68:69], 0, s[18:19]
	v_lshl_add_u64 v[72:73], v[70:71], 0, v[84:85]
	v_lshl_add_u64 v[70:71], v[70:71], 0, v[86:87]
	global_load_dword v170, v[72:73], off
	global_load_dword v168, v[70:71], off
	v_lshl_add_u64 v[72:73], v[68:69], 0, v[84:85]
	v_lshl_add_u64 v[68:69], v[68:69], 0, v[86:87]
	global_load_dword v169, v[68:69], off
	v_or_b32_e32 v68, 3, v2
	v_mad_u64_u32 v[68:69], s[12:13], v68, s14, v[100:101]
	v_lshl_add_u64 v[70:71], v[68:69], 0, s[16:17]
	global_load_dword v171, v[72:73], off
	v_lshl_add_u64 v[68:69], v[68:69], 0, s[18:19]
	v_lshl_add_u64 v[72:73], v[70:71], 0, v[84:85]
	v_lshl_add_u64 v[70:71], v[70:71], 0, v[86:87]
	global_load_dword v165, v[72:73], off
	global_load_dword v164, v[70:71], off
	v_lshl_add_u64 v[72:73], v[68:69], 0, v[84:85]
	v_lshl_add_u64 v[68:69], v[68:69], 0, v[86:87]
	global_load_dword v166, v[68:69], off
	v_or_b32_e32 v68, 8, v2
	v_mad_u64_u32 v[68:69], s[12:13], v68, s14, v[100:101]
	v_lshl_add_u64 v[70:71], v[68:69], 0, s[16:17]
	global_load_dword v167, v[72:73], off
	v_lshl_add_u64 v[68:69], v[68:69], 0, s[18:19]
	v_lshl_add_u64 v[72:73], v[70:71], 0, v[84:85]
	v_lshl_add_u64 v[70:71], v[70:71], 0, v[86:87]
	global_load_dword v162, v[72:73], off
	global_load_dword v160, v[70:71], off
	v_lshl_add_u64 v[72:73], v[68:69], 0, v[84:85]
; __device__ __forceinline__ int crow(int r, int hi) { return (r & 3) + 8 * (r >> 2) + 4 * hi; }
; __device__ __forceinline__ void unit(const bf16_t* proj, const float* stats  , const float* lng, const float* lnb, const float* sw, const float* sb, bf16_t* Y2, int un, LAS unsigned char* lds) {
;     ...
;     for (int r = 0; r < 16; ++r) { const int tr = tb * 32 + att::crow(r, hi), bt = R0 + tr; bias[r] = sb[g * 128 + tr];
; #pragma unroll
;         for (int d = 0; d < 2; ++d) { const int ch = g * 128 + (2 * eh + d) * 32 + (r32 & ~1); uu[r * 2 + d] = *(const unsigned*)(proj + (size_t)bt * NC + C_UC + ch); zq[r * 2 + d] = *(const unsigned*)(proj + (size_t)bt * NC + C_ZC + ch); } }
	v_lshl_add_u64 v[68:69], v[68:69], 0, v[86:87]
	global_load_dword v161, v[68:69], off
	v_or_b32_e32 v68, 9, v2
	v_mad_u64_u32 v[68:69], s[12:13], v68, s14, v[100:101]
	v_lshl_add_u64 v[70:71], v[68:69], 0, s[16:17]
	global_load_dword v163, v[72:73], off
	v_lshl_add_u64 v[68:69], v[68:69], 0, s[18:19]
	v_lshl_add_u64 v[72:73], v[70:71], 0, v[84:85]
	v_lshl_add_u64 v[70:71], v[70:71], 0, v[86:87]
	global_load_dword v157, v[72:73], off
	global_load_dword v156, v[70:71], off
	v_lshl_add_u64 v[72:73], v[68:69], 0, v[84:85]
	v_lshl_add_u64 v[68:69], v[68:69], 0, v[86:87]
	global_load_dword v158, v[68:69], off
	v_or_b32_e32 v68, 10, v2
	v_mad_u64_u32 v[68:69], s[12:13], v68, s14, v[100:101]
	v_lshl_add_u64 v[70:71], v[68:69], 0, s[16:17]
	global_load_dword v159, v[72:73], off
	v_lshl_add_u64 v[68:69], v[68:69], 0, s[18:19]
	v_lshl_add_u64 v[72:73], v[70:71], 0, v[84:85]
	v_lshl_add_u64 v[70:71], v[70:71], 0, v[86:87]
	global_load_dword v154, v[72:73], off
	global_load_dword v152, v[70:71], off
	v_lshl_add_u64 v[72:73], v[68:69], 0, v[84:85]
	v_lshl_add_u64 v[68:69], v[68:69], 0, v[86:87]
	global_load_dword v153, v[68:69], off
	v_or_b32_e32 v68, 11, v2
	v_mad_u64_u32 v[68:69], s[12:13], v68, s14, v[100:101]
	v_lshl_add_u64 v[70:71], v[68:69], 0, s[16:17]
	global_load_dword v155, v[72:73], off
	v_lshl_add_u64 v[68:69], v[68:69], 0, s[18:19]
	v_lshl_add_u64 v[72:73], v[70:71], 0, v[84:85]
	v_lshl_add_u64 v[70:71], v[70:71], 0, v[86:87]
	global_load_dword v149, v[72:73], off
	global_load_dword v148, v[70:71], off
	v_lshl_add_u64 v[72:73], v[68:69], 0, v[84:85]
	v_lshl_add_u64 v[68:69], v[68:69], 0, v[86:87]
	global_load_dword v150, v[68:69], off
	v_or_b32_e32 v68, 16, v2
	v_mad_u64_u32 v[68:69], s[12:13], v68, s14, v[100:101]
	v_lshl_add_u64 v[70:71], v[68:69], 0, s[16:17]
	v_lshl_add_u64 v[68:69], v[68:69], 0, s[18:19]
	v_lshl_add_u64 v[88:89], v[70:71], 0, v[84:85]
	global_load_dword v151, v[72:73], off
	global_load_dword v146, v[88:89], off
	v_lshl_add_u64 v[88:89], v[68:69], 0, v[84:85]
	v_lshl_add_u64 v[70:71], v[70:71], 0, v[86:87]
	v_lshl_add_u64 v[68:69], v[68:69], 0, v[86:87]
	global_load_dword v143, v[70:71], off
	global_load_dword v144, v[68:69], off
	v_or_b32_e32 v68, 17, v2
	v_mad_u64_u32 v[68:69], s[12:13], v68, s14, v[100:101]
	v_lshl_add_u64 v[70:71], v[68:69], 0, s[16:17]
	global_load_dword v147, v[88:89], off
	v_lshl_add_u64 v[68:69], v[68:69], 0, s[18:19]
	v_lshl_add_u64 v[88:89], v[70:71], 0, v[84:85]
	v_lshl_add_u64 v[70:71], v[70:71], 0, v[86:87]
	global_load_dword v140, v[88:89], off
	global_load_dword v139, v[70:71], off
	v_lshl_add_u64 v[88:89], v[68:69], 0, v[84:85]
	v_lshl_add_u64 v[68:69], v[68:69], 0, v[86:87]
	global_load_dword v141, v[68:69], off
	v_or_b32_e32 v68, 18, v2
	v_mad_u64_u32 v[68:69], s[12:13], v68, s14, v[100:101]
	v_lshl_add_u64 v[70:71], v[68:69], 0, s[16:17]
	global_load_dword v142, v[88:89], off
	v_lshl_add_u64 v[68:69], v[68:69], 0, s[18:19]
	v_lshl_add_u64 v[88:89], v[70:71], 0, v[84:85]
	v_lshl_add_u64 v[70:71], v[70:71], 0, v[86:87]
	global_load_dword v137, v[88:89], off
	global_load_dword v135, v[70:71], off
	v_lshl_add_u64 v[88:89], v[68:69], 0, v[84:85]
	v_lshl_add_u64 v[68:69], v[68:69], 0, v[86:87]
	global_load_dword v136, v[68:69], off
	v_or_b32_e32 v68, 19, v2
	v_mad_u64_u32 v[68:69], s[12:13], v68, s14, v[100:101]
	v_lshl_add_u64 v[70:71], v[68:69], 0, s[16:17]
	global_load_dword v138, v[88:89], off
	v_lshl_add_u64 v[68:69], v[68:69], 0, s[18:19]
	v_lshl_add_u64 v[88:89], v[70:71], 0, v[84:85]
	v_lshl_add_u64 v[70:71], v[70:71], 0, v[86:87]
	global_load_dword v133, v[88:89], off
	global_load_dword v131, v[70:71], off
	v_lshl_add_u64 v[88:89], v[68:69], 0, v[84:85]
	v_lshlrev_b32_e32 v1, 2, v1
	global_load_dword v134, v[88:89], off
	v_lshl_add_u64 v[68:69], v[68:69], 0, v[86:87]
	v_or_b32_e32 v88, 24, v2
	global_load_dwordx4 v[80:83], v1, s[6:7]
	global_load_dwordx4 v[76:79], v1, s[6:7] offset:32
	global_load_dwordx4 v[72:75], v1, s[6:7] offset:64
	global_load_dword v132, v[68:69], off
	v_ashrrev_i32_e32 v185, 4, v176
	global_load_dwordx4 v[68:71], v1, s[6:7] offset:96
	v_mad_u64_u32 v[88:89], s[6:7], v88, s14, v[100:101]
	v_lshl_add_u64 v[90:91], v[88:89], 0, s[16:17]
	v_lshl_add_u64 v[88:89], v[88:89], 0, s[18:19]
	v_lshl_add_u64 v[92:93], v[90:91], 0, v[84:85]
	v_lshl_add_u64 v[90:91], v[90:91], 0, v[86:87]
	global_load_dword v129, v[92:93], off
	global_load_dword v127, v[90:91], off
	v_lshl_add_u64 v[92:93], v[88:89], 0, v[84:85]
	v_lshl_add_u64 v[88:89], v[88:89], 0, v[86:87]
	v_or_b32_e32 v1, 25, v2
	global_load_dword v128, v[88:89], off
	v_mad_u64_u32 v[88:89], s[6:7], v1, s14, v[100:101]
	v_lshl_add_u64 v[90:91], v[88:89], 0, s[16:17]
	global_load_dword v130, v[92:93], off
	v_lshl_add_u64 v[88:89], v[88:89], 0, s[18:19]
	v_lshl_add_u64 v[92:93], v[90:91], 0, v[84:85]
	v_lshl_add_u64 v[90:91], v[90:91], 0, v[86:87]
	global_load_dword v125, v[92:93], off
	global_load_dword v123, v[90:91], off
	v_lshl_add_u64 v[92:93], v[88:89], 0, v[84:85]
	v_lshl_add_u64 v[88:89], v[88:89], 0, v[86:87]
	v_or_b32_e32 v1, 26, v2
	global_load_dword v124, v[88:89], off
	v_mad_u64_u32 v[88:89], s[6:7], v1, s14, v[100:101]
	v_lshl_add_u64 v[90:91], v[88:89], 0, s[16:17]
	global_load_dword v126, v[92:93], off
	v_lshl_add_u64 v[88:89], v[88:89], 0, s[18:19]
	v_lshl_add_u64 v[92:93], v[90:91], 0, v[84:85]
	v_lshl_add_u64 v[90:91], v[90:91], 0, v[86:87]
	global_load_dword v121, v[92:93], off
	global_load_dword v119, v[90:91], off
	v_lshl_add_u64 v[92:93], v[88:89], 0, v[84:85]
	v_lshl_add_u64 v[88:89], v[88:89], 0, v[86:87]
	v_or_b32_e32 v1, 27, v2
	global_load_dword v120, v[88:89], off
; __device__ __forceinline__ void unit(const bf16_t* proj, const float* stats  , const float* lng, const float* lnb, const float* sw, const float* sb, bf16_t* Y2, int un, LAS unsigned char* lds) {
;     ...
;     { const int sr = tid >> 4, sc = (tid & 15) * 8, ch = g * 128 + sc;
;       const f32x4 g0 = *(const f32x4*)(lng + ch), g1 = *(const f32x4*)(lng + ch + 4), b0 = *(const f32x4*)(lnb + ch), b1 = *(const f32x4*)(lnb + ch + 4);
;       float mus[4], rss[4];
;       { float2 pp[4];
; #pragma unroll
;         for (int q = 0; q < 4; ++q) pp[q] = *(const float2*)(stats + ((size_t)(R0 + sr + 32 * q) * 16 + (tid & 15)) * 2);
;         asm volatile("" ::: "memory");
; #pragma unroll
;         for (int q = 0; q < 4; ++q) { float s1 = pp[q].x, s2 = pp[q].y;
; #pragma unroll
;             for (int off = 1; off < 16; off <<= 1) { s1 += __shfl_xor(s1, off); s2 += __shfl_xor(s2, off); }
;             mus[q] = s1 * (1.0f / 1024.0f); rss[q] = __builtin_amdgcn_rsqf(fmaxf(s2 * (1.0f / 1024.0f) - mus[q] * mus[q], 0.f) + LN_EPS); } }
; #pragma unroll
;       for (int q = 0; q < 4; ++q) { const int s = sr + 32 * q, row = R0 + s; const u32x4 vv = *(const u32x4*)(proj + (size_t)row * NC + C_VC + ch);
	v_mad_u64_u32 v[88:89], s[6:7], v1, s14, v[100:101]
	v_lshl_add_u64 v[90:91], v[88:89], 0, s[16:17]
	v_lshl_add_u64 v[88:89], v[88:89], 0, s[18:19]
	global_load_dword v122, v[92:93], off
	v_lshl_add_u64 v[92:93], v[90:91], 0, v[84:85]
	v_lshl_add_u64 v[84:85], v[88:89], 0, v[84:85]
	global_load_dword v109, v[92:93], off
	global_load_dword v115, v[84:85], off
	v_lshl_add_u64 v[84:85], v[90:91], 0, v[86:87]
	global_load_dword v1, v[84:85], off
	v_lshl_add_u64 v[84:85], v[88:89], 0, v[86:87]
	global_load_dword v107, v[84:85], off
	v_and_b32_e32 v84, 15, v176
	v_lshlrev_b32_e32 v102, 3, v84
	v_or_b32_e32 v191, s2, v102
	v_lshlrev_b32_e32 v96, 2, v191
	global_load_dwordx4 v[84:87], v96, s[0:1] offset:16
	global_load_dwordx4 v[92:95], v96, s[0:1]
	global_load_dwordx4 v[88:91], v96, s[4:5] offset:16
	s_nop 0
	global_load_dwordx4 v[96:99], v96, s[4:5]
	v_add_u32_e32 v110, s11, v185
	v_readlane_b32 s0, v254, 37
	v_mov_b32_e32 v103, v3
	v_readlane_b32 s1, v254, 38
	v_ashrrev_i32_e32 v111, 31, v110
	v_lshlrev_b64 v[104:105], 7, v[110:111]
	v_lshl_add_u64 v[102:103], s[0:1], 0, v[102:103]
	v_lshl_add_u64 v[112:113], v[102:103], 0, v[104:105]
	global_load_dwordx2 v[104:105], v[112:113], off
	s_movk_i32 s0, 0x2000
	v_add_co_u32_e32 v116, vcc, s0, v112
	s_movk_i32 s0, 0x3000
	s_nop 0
	v_addc_co_u32_e32 v117, vcc, 0, v113, vcc
	global_load_dwordx2 v[102:103], v[116:117], off offset:-4096
	global_load_dwordx2 v[186:187], v[116:117], off
	v_add_co_u32_e32 v112, vcc, s0, v112
	v_and_b32_e32 v106, 64, v229
	s_nop 0
	v_addc_co_u32_e32 v113, vcc, 0, v113, vcc
	v_add_u32_e32 v106, 64, v106
	v_xor_b32_e32 v108, 1, v229
	v_cmp_lt_i32_e32 vcc, v108, v106
	global_load_dwordx2 v[188:189], v[112:113], off
	s_mov_b32 s0, 0x3a800000
	v_cndmask_b32_e32 v108, v229, v108, vcc
	v_lshlrev_b32_e32 v145, 2, v108
	v_xor_b32_e32 v108, 2, v229
	v_cmp_lt_i32_e32 vcc, v108, v106
	s_movk_i32 s4, 0x4000
	v_and_b32_e32 v184, 63, v176
	v_cndmask_b32_e32 v108, v229, v108, vcc
	v_lshlrev_b32_e32 v111, 2, v108
	v_xor_b32_e32 v108, 4, v229
	v_cmp_lt_i32_e32 vcc, v108, v106
	s_cmpk_gt_u32 s10, 0xff
	s_waitcnt vmcnt(3)
	ds_bpermute_b32 v112, v145, v104
	ds_bpermute_b32 v113, v145, v105
	v_cndmask_b32_e32 v108, v229, v108, vcc
	v_lshlrev_b32_e32 v190, 2, v108
	v_xor_b32_e32 v108, 8, v229
	v_cmp_lt_i32_e32 vcc, v108, v106
	s_waitcnt lgkmcnt(0)
	v_pk_add_f32 v[104:105], v[104:105], v[112:113]
	ds_bpermute_b32 v112, v111, v104
	ds_bpermute_b32 v113, v111, v105
	v_cndmask_b32_e32 v106, v229, v108, vcc
	v_lshlrev_b32_e32 v106, 2, v106
	s_waitcnt lgkmcnt(0)
	v_pk_add_f32 v[104:105], v[104:105], v[112:113]
	ds_bpermute_b32 v112, v190, v104
	ds_bpermute_b32 v113, v190, v105
	s_waitcnt lgkmcnt(0)
	v_pk_add_f32 v[104:105], v[104:105], v[112:113]
	ds_bpermute_b32 v112, v106, v104
	ds_bpermute_b32 v113, v106, v105
	s_waitcnt lgkmcnt(0)
	v_pk_add_f32 v[104:105], v[104:105], v[112:113]
	s_nop 0
	v_pk_mul_f32 v[116:117], v[104:105], s[0:1] op_sel_hi:[1,0]
	s_waitcnt vmcnt(2)
	ds_bpermute_b32 v105, v145, v103
	v_fma_f32 v104, -v116, v116, v117
	v_max_f32_e32 v104, 0, v104
	v_add_f32_e32 v104, 0x3727c5ac, v104
	v_rsq_f32_e32 v118, v104
	ds_bpermute_b32 v104, v145, v102
	s_waitcnt lgkmcnt(0)
	v_pk_add_f32 v[102:103], v[102:103], v[104:105]
	ds_bpermute_b32 v104, v111, v102
	ds_bpermute_b32 v105, v111, v103
	s_waitcnt lgkmcnt(0)
	v_pk_add_f32 v[102:103], v[102:103], v[104:105]
	ds_bpermute_b32 v104, v190, v102
	ds_bpermute_b32 v105, v190, v103
	s_waitcnt lgkmcnt(0)
	v_pk_add_f32 v[102:103], v[102:103], v[104:105]
	ds_bpermute_b32 v104, v106, v102
	ds_bpermute_b32 v105, v106, v103
	s_waitcnt lgkmcnt(0)
	v_pk_add_f32 v[102:103], v[102:103], v[104:105]
	s_nop 0
	v_pk_mul_f32 v[112:113], v[102:103], s[0:1] op_sel_hi:[1,0]
	s_waitcnt vmcnt(1)
	ds_bpermute_b32 v103, v145, v187
	v_fma_f32 v102, -v112, v112, v113
	v_max_f32_e32 v102, 0, v102
	v_add_f32_e32 v102, 0x3727c5ac, v102
	v_rsq_f32_e32 v114, v102
	ds_bpermute_b32 v102, v145, v186
	s_waitcnt lgkmcnt(0)
	v_pk_add_f32 v[102:103], v[186:187], v[102:103]
	ds_bpermute_b32 v104, v111, v102
	ds_bpermute_b32 v105, v111, v103
	s_waitcnt lgkmcnt(0)
	v_pk_add_f32 v[102:103], v[102:103], v[104:105]
	ds_bpermute_b32 v104, v190, v102
	ds_bpermute_b32 v105, v190, v103
	s_waitcnt lgkmcnt(0)
	v_pk_add_f32 v[102:103], v[102:103], v[104:105]
	ds_bpermute_b32 v104, v106, v102
	ds_bpermute_b32 v105, v106, v103
	s_waitcnt lgkmcnt(0)
	v_pk_add_f32 v[102:103], v[102:103], v[104:105]
	s_nop 0
	v_pk_mul_f32 v[102:103], v[102:103], s[0:1] op_sel_hi:[1,0]
	s_waitcnt vmcnt(0)
	ds_bpermute_b32 v105, v145, v189
	v_fma_f32 v104, -v102, v102, v103
	v_max_f32_e32 v104, 0, v104
	v_add_f32_e32 v104, 0x3727c5ac, v104
	v_rsq_f32_e32 v108, v104
	ds_bpermute_b32 v104, v145, v188
	s_waitcnt lgkmcnt(0)
	v_pk_add_f32 v[104:105], v[188:189], v[104:105]
	ds_bpermute_b32 v186, v111, v104
	ds_bpermute_b32 v187, v111, v105
	v_lshlrev_b32_e32 v111, 1, v185
	v_bfe_u32 v188, v176, 2, 2
	s_waitcnt lgkmcnt(0)
	v_pk_add_f32 v[104:105], v[104:105], v[186:187]
	ds_bpermute_b32 v186, v190, v104
	ds_bpermute_b32 v187, v190, v105
	s_waitcnt lgkmcnt(0)
	v_pk_add_f32 v[104:105], v[104:105], v[186:187]
	ds_bpermute_b32 v186, v106, v104
	ds_bpermute_b32 v187, v106, v105
	s_waitcnt lgkmcnt(0)
	v_pk_add_f32 v[104:105], v[104:105], v[186:187]
	v_and_b32_e32 v187, 8, v111
	v_lshrrev_b32_e32 v111, 1, v185
	v_and_b32_e32 v186, 3, v185
	v_and_or_b32 v111, v111, 4, v186
	v_pk_mul_f32 v[104:105], v[104:105], s[0:1] op_sel_hi:[1,0]
	v_lshlrev_b32_e32 v189, 6, v111
	v_mad_i64_i32 v[192:193], s[0:1], v110, s14, v[100:101]
	v_lshlrev_b32_e32 v110, 1, v191
	v_mov_b32_e32 v111, v3
	v_lshl_add_u64 v[192:193], v[192:193], 0, v[110:111]
	v_add_co_u32_e32 v192, vcc, s4, v192
	v_lshlrev_b32_e32 v186, 4, v176
	s_nop 0
	v_addc_co_u32_e32 v193, vcc, 0, v193, vcc
	global_load_dwordx4 v[196:199], v[192:193], off offset:2048
	v_and_b32_e32 v190, 48, v186
	v_fma_f32 v106, -v104, v104, v105
	v_max_f32_e32 v106, 0, v106
	v_add_f32_e32 v106, 0x3727c5ac, v106
	v_rsq_f32_e32 v106, v106
	s_waitcnt vmcnt(0)
; __device__ __forceinline__ unsigned cvt_pk_bf16(float lo, float hi) { f32x2_t v = {lo, hi}; bf16x2_t b = __builtin_convertvector(v, bf16x2_t); return __builtin_bit_cast(unsigned, b); }
; #define LAS __attribute__((address_space(3)))
; __device__ __forceinline__ float bflo(unsigned w) { return __uint_as_float(w << 16); }
; __device__ __forceinline__ float bfhi(unsigned w) { return __uint_as_float(w & 0xffff0000u); }
; __device__ __forceinline__ int v_st(int k, int c) { const int kk = (k & ~0xC) | ((k & 4) << 1) | ((k & 8) >> 1); return ((kk >> 3) * 4 + (c >> 5)) * 512 + ((kk & 7) * 32 + (c & 31)) * 2; }
; __device__ __forceinline__ void unit(const bf16_t* proj, const float* stats  , const float* lng, const float* lnb, const float* sw, const float* sb, bf16_t* Y2, int un, LAS unsigned char* lds) {
;     ...
;       for (int q = 0; q < 4; ++q) { const int s = sr + 32 * q, row = R0 + s; const u32x4 vv = *(const u32x4*)(proj + (size_t)row * NC + C_VC + ch);
;           const float mu = mus[q], rs = rss[q];
;           u32x4 w; w.x = pg8::cvt_pk_bf16((bflo(vv.x) - mu) * rs * g0[0] + b0[0], (bfhi(vv.x) - mu) * rs * g0[1] + b0[1]); w.y = pg8::cvt_pk_bf16((bflo(vv.y) - mu) * rs * g0[2] + b0[2], (bfhi(vv.y) - mu) * rs * g0[3] + b0[3]);
;           w.z = pg8::cvt_pk_bf16((bflo(vv.z) - mu) * rs * g1[0] + b1[0], (bfhi(vv.z) - mu) * rs * g1[1] + b1[1]); w.w = pg8::cvt_pk_bf16((bflo(vv.w) - mu) * rs * g1[2] + b1[2], (bfhi(vv.w) - mu) * rs * g1[3] + b1[3]);
;           *(LAS u32x4*)(lds + (s >> 6) * att::SHM_V + att::v_st(s & 63, sc)) = w; } }
	v_lshlrev_b32_e32 v192, 16, v196
	v_and_b32_e32 v193, 0xffff0000, v196
	v_pk_add_f32 v[192:193], v[192:193], v[116:117] op_sel_hi:[1,0] neg_lo:[0,1] neg_hi:[0,1]
	s_nop 0
	v_pk_mul_f32 v[192:193], v[118:119], v[192:193] op_sel_hi:[0,1]
	v_pk_fma_f32 v[192:193], v[92:93], v[192:193], v[96:97]
	s_nop 0
	v_cvt_pk_bf16_f32 v196, v192, v193
	v_lshlrev_b32_e32 v192, 16, v197
	v_and_b32_e32 v193, 0xffff0000, v197
	v_pk_add_f32 v[192:193], v[192:193], v[116:117] op_sel_hi:[1,0] neg_lo:[0,1] neg_hi:[0,1]
	s_nop 0
	v_pk_mul_f32 v[192:193], v[118:119], v[192:193] op_sel_hi:[0,1]
	v_pk_fma_f32 v[192:193], v[94:95], v[192:193], v[98:99]
	s_nop 0
	v_cvt_pk_bf16_f32 v197, v192, v193
	v_lshlrev_b32_e32 v192, 16, v198
	v_and_b32_e32 v193, 0xffff0000, v198
	v_pk_add_f32 v[192:193], v[192:193], v[116:117] op_sel_hi:[1,0] neg_lo:[0,1] neg_hi:[0,1]
	s_nop 0
	v_pk_mul_f32 v[192:193], v[118:119], v[192:193] op_sel_hi:[0,1]
	v_pk_fma_f32 v[192:193], v[84:85], v[192:193], v[88:89]
	s_nop 0
	v_cvt_pk_bf16_f32 v198, v192, v193
	v_lshlrev_b32_e32 v192, 16, v199
	v_and_b32_e32 v193, 0xffff0000, v199
	v_pk_add_f32 v[116:117], v[192:193], v[116:117] op_sel_hi:[1,0] neg_lo:[0,1] neg_hi:[0,1]
	s_nop 0
	v_pk_mul_f32 v[116:117], v[118:119], v[116:117] op_sel_hi:[0,1]
	v_pk_fma_f32 v[116:117], v[86:87], v[116:117], v[90:91]
	s_nop 0
	v_cvt_pk_bf16_f32 v199, v116, v117
	v_lshlrev_b32_e32 v116, 8, v185
	v_and_b32_e32 v117, 0xffffc000, v116
	v_and_or_b32 v116, v185, 48, v187
	v_lshrrev_b32_e32 v116, 1, v116
	v_or_b32_e32 v116, v116, v188
	v_lshlrev_b32_e32 v116, 9, v116
	v_add3_u32 v117, 0, v117, v116
	v_add3_u32 v117, v117, v189, v190
	ds_write_b128 v117, v[196:199]
	v_add_u32_e32 v117, 32, v185
	v_add_u32_e32 v118, s11, v117
	v_mad_i64_i32 v[192:193], s[0:1], v118, s14, v[100:101]
	v_lshl_add_u64 v[192:193], v[192:193], 0, v[110:111]
	v_add_co_u32_e32 v192, vcc, s4, v192
	s_nop 1
	v_addc_co_u32_e32 v193, vcc, 0, v193, vcc
	global_load_dwordx4 v[196:199], v[192:193], off offset:2048
	s_waitcnt vmcnt(0)
	v_lshlrev_b32_e32 v192, 16, v196
	v_and_b32_e32 v193, 0xffff0000, v196
	v_pk_add_f32 v[192:193], v[192:193], v[112:113] op_sel_hi:[1,0] neg_lo:[0,1] neg_hi:[0,1]
	s_nop 0
	v_pk_mul_f32 v[192:193], v[114:115], v[192:193] op_sel_hi:[0,1]
	v_pk_fma_f32 v[192:193], v[92:93], v[192:193], v[96:97]
	s_nop 0
	v_cvt_pk_bf16_f32 v196, v192, v193
	v_lshlrev_b32_e32 v192, 16, v197
	v_and_b32_e32 v193, 0xffff0000, v197
	v_pk_add_f32 v[192:193], v[192:193], v[112:113] op_sel_hi:[1,0] neg_lo:[0,1] neg_hi:[0,1]
	s_nop 0
	v_pk_mul_f32 v[192:193], v[114:115], v[192:193] op_sel_hi:[0,1]
	v_pk_fma_f32 v[192:193], v[94:95], v[192:193], v[98:99]
	s_nop 0
	v_cvt_pk_bf16_f32 v197, v192, v193
	v_lshlrev_b32_e32 v192, 16, v198
	v_and_b32_e32 v193, 0xffff0000, v198
	v_pk_add_f32 v[192:193], v[192:193], v[112:113] op_sel_hi:[1,0] neg_lo:[0,1] neg_hi:[0,1]
	s_nop 0
	v_pk_mul_f32 v[192:193], v[114:115], v[192:193] op_sel_hi:[0,1]
	v_pk_fma_f32 v[192:193], v[84:85], v[192:193], v[88:89]
	s_nop 0
	v_cvt_pk_bf16_f32 v198, v192, v193
	v_lshlrev_b32_e32 v192, 16, v199
	v_and_b32_e32 v193, 0xffff0000, v199
	v_pk_add_f32 v[112:113], v[192:193], v[112:113] op_sel_hi:[1,0] neg_lo:[0,1] neg_hi:[0,1]
	s_nop 0
	v_pk_mul_f32 v[112:113], v[114:115], v[112:113] op_sel_hi:[0,1]
	v_pk_fma_f32 v[112:113], v[86:87], v[112:113], v[90:91]
	v_add_u32_e32 v114, 64, v185
	v_cvt_pk_bf16_f32 v199, v112, v113
	v_and_or_b32 v113, v117, 48, v187
	v_lshrrev_b32_e32 v113, 1, v113
	v_lshlrev_b32_e32 v112, 8, v117
	v_or_b32_e32 v113, v113, v188
	v_and_b32_e32 v112, 0xffffc000, v112
	v_lshlrev_b32_e32 v113, 9, v113
	v_add3_u32 v112, 0, v112, v113
	v_add3_u32 v112, v112, v189, v190
	ds_write_b128 v112, v[196:199]
	v_add_u32_e32 v112, s11, v114
	v_mad_i64_i32 v[112:113], s[0:1], v112, s14, v[100:101]
	v_lshl_add_u64 v[112:113], v[112:113], 0, v[110:111]
	v_add_co_u32_e32 v112, vcc, s4, v112
	s_nop 1
	v_addc_co_u32_e32 v113, vcc, 0, v113, vcc
	global_load_dwordx4 v[196:199], v[112:113], off offset:2048
	s_waitcnt vmcnt(0)
	v_lshlrev_b32_e32 v112, 16, v196
	v_and_b32_e32 v113, 0xffff0000, v196
	v_pk_add_f32 v[112:113], v[112:113], v[102:103] op_sel_hi:[1,0] neg_lo:[0,1] neg_hi:[0,1]
	s_nop 0
	v_pk_mul_f32 v[112:113], v[108:109], v[112:113] op_sel_hi:[0,1]
	v_pk_fma_f32 v[112:113], v[92:93], v[112:113], v[96:97]
	s_nop 0
	v_cvt_pk_bf16_f32 v196, v112, v113
	v_lshlrev_b32_e32 v112, 16, v197
	v_and_b32_e32 v113, 0xffff0000, v197
	v_pk_add_f32 v[112:113], v[112:113], v[102:103] op_sel_hi:[1,0] neg_lo:[0,1] neg_hi:[0,1]
	s_nop 0
	v_pk_mul_f32 v[112:113], v[108:109], v[112:113] op_sel_hi:[0,1]
	v_pk_fma_f32 v[112:113], v[94:95], v[112:113], v[98:99]
	s_nop 0
	v_cvt_pk_bf16_f32 v197, v112, v113
	v_lshlrev_b32_e32 v112, 16, v198
	v_and_b32_e32 v113, 0xffff0000, v198
	v_pk_add_f32 v[112:113], v[112:113], v[102:103] op_sel_hi:[1,0] neg_lo:[0,1] neg_hi:[0,1]
	s_nop 0
	v_pk_mul_f32 v[112:113], v[108:109], v[112:113] op_sel_hi:[0,1]
	v_pk_fma_f32 v[112:113], v[84:85], v[112:113], v[88:89]
	s_nop 0
	v_cvt_pk_bf16_f32 v198, v112, v113
	v_lshlrev_b32_e32 v112, 16, v199
	v_and_b32_e32 v113, 0xffff0000, v199
	v_pk_add_f32 v[102:103], v[112:113], v[102:103] op_sel_hi:[1,0] neg_lo:[0,1] neg_hi:[0,1]
	s_nop 0
	v_pk_mul_f32 v[102:103], v[108:109], v[102:103] op_sel_hi:[0,1]
	v_pk_fma_f32 v[102:103], v[86:87], v[102:103], v[90:91]
	v_add_u32_e32 v108, 0x60, v185
	v_cvt_pk_bf16_f32 v199, v102, v103
	v_lshlrev_b32_e32 v102, 8, v114
	v_and_b32_e32 v102, 0xffffc000, v102
	v_add3_u32 v102, 0, v102, v116
	v_add3_u32 v102, v102, v189, v190
	ds_write_b128 v102, v[196:199]
	v_add_u32_e32 v102, s11, v108
	v_mad_i64_i32 v[100:101], s[0:1], v102, s14, v[100:101]
	v_lshl_add_u64 v[100:101], v[100:101], 0, v[110:111]
	v_add_co_u32_e32 v100, vcc, s4, v100
	s_cselect_b64 s[0:1], -1, 0
	s_nop 0
	v_addc_co_u32_e32 v101, vcc, 0, v101, vcc
	global_load_dwordx4 v[100:103], v[100:101], off offset:2048
	v_cmp_le_u32_e32 vcc, v183, v182
	s_mov_b64 s[4:5], -1
	s_waitcnt vmcnt(0)
; __device__ __forceinline__ unsigned cvt_pk_bf16(float lo, float hi) { f32x2_t v = {lo, hi}; bf16x2_t b = __builtin_convertvector(v, bf16x2_t); return __builtin_bit_cast(unsigned, b); }
; #define LAS __attribute__((address_space(3)))
; __device__ __forceinline__ float bflo(unsigned w) { return __uint_as_float(w << 16); }
; __device__ __forceinline__ float bfhi(unsigned w) { return __uint_as_float(w & 0xffff0000u); }
; __device__ __forceinline__ void unit(const bf16_t* proj, const float* stats  , const float* lng, const float* lnb, const float* sw, const float* sb, bf16_t* Y2, int un, LAS unsigned char* lds) {
;     ...
;           u32x4 w; w.x = pg8::cvt_pk_bf16((bflo(vv.x) - mu) * rs * g0[0] + b0[0], (bfhi(vv.x) - mu) * rs * g0[1] + b0[1]); w.y = pg8::cvt_pk_bf16((bflo(vv.y) - mu) * rs * g0[2] + b0[2], (bfhi(vv.y) - mu) * rs * g0[3] + b0[3]);
;           w.z = pg8::cvt_pk_bf16((bflo(vv.z) - mu) * rs * g1[0] + b1[0], (bfhi(vv.z) - mu) * rs * g1[1] + b1[1]); w.w = pg8::cvt_pk_bf16((bflo(vv.w) - mu) * rs * g1[2] + b1[2], (bfhi(vv.w) - mu) * rs * g1[3] + b1[3]);
;           *(LAS u32x4*)(lds + (s >> 6) * att::SHM_V + att::v_st(s & 63, sc)) = w; } }
;     __syncthreads();
;     att::f32x16 o0 = att::f32x16{}, o1 = att::f32x16{};
;     LAS const unsigned char* vb = lds + att::v_rd_base(lane);
; #pragma unroll
;     for (int st = 0; st < 2; ++st) {
;         if (st * 64 > tb * 32 + 31) continue;
;         att::bf16x8 pa[4];
; #pragma unroll
;         for (int k = 0; k < 4; ++k) { const int s0 = st * 64 + 16 * k + hi * 8; const f32x4 w0 = wv[2 * (st * 4 + k)], w1 = wv[2 * (st * 4 + k) + 1];
;             float x[8] = {w0[0], w0[1], w0[2], w0[3], w1[0], w1[1], w1[2], w1[3]};
; #pragma unroll
;             for (int j = 0; j < 8; ++j) x[j] = (s0 + j <= t) ? x[j] : 0.f;
;             u32x4 p; p.x = pg8::cvt_pk_bf16(x[0], x[1]); p.y = pg8::cvt_pk_bf16(x[2], x[3]); p.z = pg8::cvt_pk_bf16(x[4], x[5]); p.w = pg8::cvt_pk_bf16(x[6], x[7]); pa[k] = __builtin_bit_cast(att::bf16x8, p); }
;         if (eh == 0) { att::pv_one<0>(o0, vb + st * att::SHM_V, pa[0], pa[1], pa[2], pa[3]); att::pv_one<1>(o1, vb + st * att::SHM_V, pa[0], pa[1], pa[2], pa[3]); }
;         else         { att::pv_one<2>(o0, vb + st * att::SHM_V, pa[0], pa[1], pa[2], pa[3]); att::pv_one<3>(o1, vb + st * att::SHM_V, pa[0], pa[1], pa[2], pa[3]); }
	v_lshlrev_b32_e32 v110, 16, v100
	v_and_b32_e32 v111, 0xffff0000, v100
	v_pk_add_f32 v[110:111], v[110:111], v[104:105] op_sel_hi:[1,0] neg_lo:[0,1] neg_hi:[0,1]
	v_cndmask_b32_e32 v32, 0, v32, vcc
	v_pk_mul_f32 v[110:111], v[106:107], v[110:111] op_sel_hi:[0,1]
	v_pk_fma_f32 v[92:93], v[92:93], v[110:111], v[96:97]
	v_lshlrev_b32_e32 v96, 16, v101
	v_and_b32_e32 v97, 0xffff0000, v101
	v_pk_add_f32 v[96:97], v[96:97], v[104:105] op_sel_hi:[1,0] neg_lo:[0,1] neg_hi:[0,1]
	v_cvt_pk_bf16_f32 v92, v92, v93
	v_pk_mul_f32 v[96:97], v[106:107], v[96:97] op_sel_hi:[0,1]
	v_pk_fma_f32 v[94:95], v[94:95], v[96:97], v[98:99]
	v_cmp_lt_u32_e32 vcc, v183, v182
	v_cvt_pk_bf16_f32 v93, v94, v95
	v_lshlrev_b32_e32 v94, 16, v102
	v_and_b32_e32 v95, 0xffff0000, v102
	v_pk_add_f32 v[94:95], v[94:95], v[104:105] op_sel_hi:[1,0] neg_lo:[0,1] neg_hi:[0,1]
	v_cndmask_b32_e32 v33, 0, v33, vcc
	v_pk_mul_f32 v[94:95], v[106:107], v[94:95] op_sel_hi:[0,1]
	v_pk_fma_f32 v[84:85], v[84:85], v[94:95], v[88:89]
	s_nop 0
	v_cvt_pk_bf16_f32 v94, v84, v85
	v_lshlrev_b32_e32 v84, 16, v103
	v_and_b32_e32 v85, 0xffff0000, v103
	v_pk_add_f32 v[84:85], v[84:85], v[104:105] op_sel_hi:[1,0] neg_lo:[0,1] neg_hi:[0,1]
	s_nop 0
	v_pk_mul_f32 v[84:85], v[106:107], v[84:85] op_sel_hi:[0,1]
	v_pk_fma_f32 v[84:85], v[86:87], v[84:85], v[90:91]
	v_and_b32_e32 v86, 0xc0, v186
	v_cvt_pk_bf16_f32 v95, v84, v85
	v_and_or_b32 v85, v108, 48, v187
	v_lshrrev_b32_e32 v85, 1, v85
	v_lshlrev_b32_e32 v84, 8, v108
	v_or_b32_e32 v85, v85, v188
	v_and_b32_e32 v84, 0xffffc000, v84
	v_lshlrev_b32_e32 v85, 9, v85
	v_add3_u32 v84, 0, v84, v85
	v_add3_u32 v84, v84, v189, v190
	ds_write_b128 v84, v[92:95]
	v_lshlrev_b32_e32 v84, 3, v184
	v_and_b32_e32 v85, 24, v84
	v_lshlrev_b32_e32 v87, 1, v176
	v_and_b32_e32 v87, 32, v87
	v_and_b32_e32 v84, 0x100, v84
	v_add3_u32 v85, 0, v85, v86
	v_add3_u32 v100, v85, v87, v84
	v_or_b32_e32 v84, 2, v183
	v_cmp_le_u32_e32 vcc, v84, v182
	v_or_b32_e32 v84, 3, v183
	s_waitcnt lgkmcnt(0)
	v_cndmask_b32_e32 v34, 0, v34, vcc
	v_cmp_le_u32_e32 vcc, v84, v182
	v_or_b32_e32 v84, 4, v183
	s_barrier
	v_cndmask_b32_e32 v35, 0, v35, vcc
	v_cmp_le_u32_e32 vcc, v84, v182
	v_or_b32_e32 v84, 5, v183
	v_cvt_pk_bf16_f32 v85, v34, v35
	v_cndmask_b32_e32 v28, 0, v28, vcc
	v_cmp_le_u32_e32 vcc, v84, v182
	v_or_b32_e32 v84, 6, v183
	s_nop 0
	v_cndmask_b32_e32 v29, 0, v29, vcc
	v_cmp_le_u32_e32 vcc, v84, v182
	v_or_b32_e32 v84, 7, v183
	v_cvt_pk_bf16_f32 v86, v28, v29
	v_cndmask_b32_e32 v30, 0, v30, vcc
	v_cmp_le_u32_e32 vcc, v84, v182
	v_or_b32_e32 v28, 16, v183
	v_cvt_pk_bf16_f32 v84, v32, v33
	v_cndmask_b32_e32 v31, 0, v31, vcc
	v_cmp_le_u32_e32 vcc, v28, v182
	v_or_b32_e32 v28, 17, v183
	v_cvt_pk_bf16_f32 v87, v30, v31
	v_cndmask_b32_e32 v24, 0, v24, vcc
	v_cmp_le_u32_e32 vcc, v28, v182
	v_or_b32_e32 v28, 18, v183
	s_nop 0
	v_cndmask_b32_e32 v25, 0, v25, vcc
	v_cmp_le_u32_e32 vcc, v28, v182
	v_or_b32_e32 v28, 19, v183
	v_cvt_pk_bf16_f32 v88, v24, v25
	v_cndmask_b32_e32 v26, 0, v26, vcc
	v_cmp_le_u32_e32 vcc, v28, v182
	v_or_b32_e32 v28, 20, v183
	s_nop 0
	v_cndmask_b32_e32 v27, 0, v27, vcc
	v_cmp_le_u32_e32 vcc, v28, v182
	v_or_b32_e32 v28, 21, v183
	v_cvt_pk_bf16_f32 v89, v26, v27
	v_cndmask_b32_e32 v20, 0, v20, vcc
	v_cmp_le_u32_e32 vcc, v28, v182
	v_or_b32_e32 v28, 22, v183
	s_nop 0
	v_cndmask_b32_e32 v21, 0, v21, vcc
	v_cmp_le_u32_e32 vcc, v28, v182
	v_or_b32_e32 v28, 23, v183
	v_cvt_pk_bf16_f32 v90, v20, v21
	v_cndmask_b32_e32 v22, 0, v22, vcc
	v_cmp_le_u32_e32 vcc, v28, v182
	v_or_b32_e32 v20, 32, v183
	s_nop 0
	v_cndmask_b32_e32 v23, 0, v23, vcc
	v_cmp_le_u32_e32 vcc, v20, v182
	v_or_b32_e32 v20, 33, v183
	v_cvt_pk_bf16_f32 v91, v22, v23
	v_cndmask_b32_e32 v16, 0, v16, vcc
	v_cmp_le_u32_e32 vcc, v20, v182
	v_or_b32_e32 v20, 34, v183
	s_nop 0
	v_cndmask_b32_e32 v17, 0, v17, vcc
	v_cmp_le_u32_e32 vcc, v20, v182
	v_or_b32_e32 v20, 35, v183
	v_cvt_pk_bf16_f32 v96, v16, v17
	v_cndmask_b32_e32 v18, 0, v18, vcc
	v_cmp_le_u32_e32 vcc, v20, v182
	v_or_b32_e32 v20, 36, v183
	s_nop 0
	v_cndmask_b32_e32 v19, 0, v19, vcc
	v_cmp_le_u32_e32 vcc, v20, v182
	v_or_b32_e32 v20, 37, v183
	v_cvt_pk_bf16_f32 v97, v18, v19
	v_cndmask_b32_e32 v12, 0, v12, vcc
	v_cmp_le_u32_e32 vcc, v20, v182
	v_or_b32_e32 v20, 38, v183
	s_nop 0
	v_cndmask_b32_e32 v13, 0, v13, vcc
	v_cmp_le_u32_e32 vcc, v20, v182
	v_or_b32_e32 v20, 39, v183
	v_cvt_pk_bf16_f32 v98, v12, v13
	v_cndmask_b32_e32 v14, 0, v14, vcc
	v_cmp_le_u32_e32 vcc, v20, v182
	v_or_b32_e32 v12, 48, v183
	s_nop 0
	v_cndmask_b32_e32 v15, 0, v15, vcc
	v_cmp_le_u32_e32 vcc, v12, v182
	v_or_b32_e32 v12, 49, v183
	v_cvt_pk_bf16_f32 v99, v14, v15
	v_cndmask_b32_e32 v8, 0, v8, vcc
	v_cmp_le_u32_e32 vcc, v12, v182
	v_or_b32_e32 v12, 50, v183
	s_nop 0
	v_cndmask_b32_e32 v9, 0, v9, vcc
	v_cmp_le_u32_e32 vcc, v12, v182
	v_or_b32_e32 v12, 51, v183
	v_cvt_pk_bf16_f32 v92, v8, v9
	v_cndmask_b32_e32 v10, 0, v10, vcc
	v_cmp_le_u32_e32 vcc, v12, v182
	v_or_b32_e32 v12, 52, v183
	s_nop 0
	v_cndmask_b32_e32 v11, 0, v11, vcc
	v_cmp_le_u32_e32 vcc, v12, v182
	v_or_b32_e32 v12, 53, v183
	v_cvt_pk_bf16_f32 v93, v10, v11
	v_cndmask_b32_e32 v4, 0, v4, vcc
	v_cmp_le_u32_e32 vcc, v12, v182
	v_or_b32_e32 v12, 54, v183
	s_nop 0
	v_cndmask_b32_e32 v5, 0, v5, vcc
	v_cmp_le_u32_e32 vcc, v12, v182
	v_or_b32_e32 v12, 55, v183
	v_cvt_pk_bf16_f32 v94, v4, v5
	v_cndmask_b32_e32 v6, 0, v6, vcc
	v_cmp_le_u32_e32 vcc, v12, v182
	s_nop 1
	v_cndmask_b32_e32 v7, 0, v7, vcc
	v_cvt_pk_bf16_f32 v95, v6, v7
	s_and_b64 vcc, exec, s[0:1]
	s_cbranch_vccz .LBB0_1379
	ds_read_b64_tr_b16 v[4:5], v100 offset:1024
	ds_read_b64_tr_b16 v[6:7], v100 offset:3072
	ds_read_b64_tr_b16 v[20:21], v100 offset:5120
	ds_read_b64_tr_b16 v[22:23], v100 offset:7168
	s_mov_b64 s[4:5], 0
	s_waitcnt lgkmcnt(2)
	s_setprio 1
	v_mfma_f32_32x32x16_bf16 v[4:19], v[84:87], v[4:7], 0
	s_waitcnt lgkmcnt(0)
	v_mfma_f32_32x32x16_bf16 v[4:19], v[88:91], v[20:23], v[4:19]
	ds_read_b64_tr_b16 v[20:21], v100 offset:9216
	ds_read_b64_tr_b16 v[22:23], v100 offset:11264
	s_waitcnt lgkmcnt(0)
	v_mfma_f32_32x32x16_bf16 v[4:19], v[96:99], v[20:23], v[4:19]
	ds_read_b64_tr_b16 v[20:21], v100 offset:13312
	ds_read_b64_tr_b16 v[22:23], v100 offset:15360
	s_waitcnt lgkmcnt(0)
	v_mfma_f32_32x32x16_bf16 v[4:19], v[92:95], v[20:23], v[4:19]
	ds_read_b64_tr_b16 v[22:23], v100 offset:3584
	ds_read_b64_tr_b16 v[20:21], v100 offset:1536
	ds_read_b64_tr_b16 v[104:105], v100 offset:7680
	ds_read_b64_tr_b16 v[102:103], v100 offset:5632
	s_waitcnt lgkmcnt(2)
	v_mfma_f32_32x32x16_bf16 v[20:35], v[84:87], v[20:23], 0
	s_waitcnt lgkmcnt(0)
	v_mfma_f32_32x32x16_bf16 v[20:35], v[88:91], v[102:105], v[20:35]
	ds_read_b64_tr_b16 v[104:105], v100 offset:11776
	ds_read_b64_tr_b16 v[102:103], v100 offset:9728
	s_waitcnt lgkmcnt(0)
	v_mfma_f32_32x32x16_bf16 v[20:35], v[96:99], v[102:105], v[20:35]
	ds_read_b64_tr_b16 v[104:105], v100 offset:15872
	ds_read_b64_tr_b16 v[102:103], v100 offset:13824
	s_waitcnt lgkmcnt(0)
	v_mfma_f32_32x32x16_bf16 v[20:35], v[92:95], v[102:105], v[20:35]
	s_setprio 0
; __device__ __forceinline__ unsigned cvt_pk_bf16(float lo, float hi) { f32x2_t v = {lo, hi}; bf16x2_t b = __builtin_convertvector(v, bf16x2_t); return __builtin_bit_cast(unsigned, b); }
; #define LAS __attribute__((address_space(3)))
; template <int D0> __device__ __forceinline__ void pv_one(f32x16& od, LAS const unsigned char* vb, bf16x8 pa0, bf16x8 pa1, bf16x8 pa2, bf16x8 pa3) {
;     const s16x4 l0 = tr_read(vb + v_rd_off(D0, 0, 0)), h0 = tr_read(vb + v_rd_off(D0, 0, 1)), l1 = tr_read(vb + v_rd_off(D0, 1, 0)), h1 = tr_read(vb + v_rd_off(D0, 1, 1));
;     const s16x4 l2 = tr_read(vb + v_rd_off(D0, 2, 0)), h2 = tr_read(vb + v_rd_off(D0, 2, 1)), l3 = tr_read(vb + v_rd_off(D0, 3, 0)), h3 = tr_read(vb + v_rd_off(D0, 3, 1));
;     ...
;     od = __builtin_amdgcn_mfma_f32_32x32x16_bf16(pa0, ATT_PK(l0, h0), od, 0, 0, 0);
;     od = __builtin_amdgcn_mfma_f32_32x32x16_bf16(pa1, ATT_PK(l1, h1), od, 0, 0, 0);
;     od = __builtin_amdgcn_mfma_f32_32x32x16_bf16(pa2, ATT_PK(l2, h2), od, 0, 0, 0);
;     od = __builtin_amdgcn_mfma_f32_32x32x16_bf16(pa3, ATT_PK(l3, h3), od, 0, 0, 0);
; __device__ __forceinline__ void unit(const bf16_t* proj, const float* stats  , const float* lng, const float* lnb, const float* sw, const float* sb, bf16_t* Y2, int un, LAS unsigned char* lds) {
;     ...
;     for (int st = 0; st < 2; ++st) {
;         if (st * 64 > tb * 32 + 31) continue;
;         att::bf16x8 pa[4];
; #pragma unroll
;         for (int k = 0; k < 4; ++k) { const int s0 = st * 64 + 16 * k + hi * 8; const f32x4 w0 = wv[2 * (st * 4 + k)], w1 = wv[2 * (st * 4 + k) + 1];
;             float x[8] = {w0[0], w0[1], w0[2], w0[3], w1[0], w1[1], w1[2], w1[3]};
; #pragma unroll
;             for (int j = 0; j < 8; ++j) x[j] = (s0 + j <= t) ? x[j] : 0.f;
;             u32x4 p; p.x = pg8::cvt_pk_bf16(x[0], x[1]); p.y = pg8::cvt_pk_bf16(x[2], x[3]); p.z = pg8::cvt_pk_bf16(x[4], x[5]); p.w = pg8::cvt_pk_bf16(x[6], x[7]); pa[k] = __builtin_bit_cast(att::bf16x8, p); }
;         if (eh == 0) { att::pv_one<0>(o0, vb + st * att::SHM_V, pa[0], pa[1], pa[2], pa[3]); att::pv_one<1>(o1, vb + st * att::SHM_V, pa[0], pa[1], pa[2], pa[3]); }
;         else         { att::pv_one<2>(o0, vb + st * att::SHM_V, pa[0], pa[1], pa[2], pa[3]); att::pv_one<3>(o1, vb + st * att::SHM_V, pa[0], pa[1], pa[2], pa[3]); }
.LBB0_1379:
	v_readlane_b32 s6, v254, 45
	s_andn2_b64 vcc, exec, s[4:5]
	v_readlane_b32 s7, v254, 46
	s_cbranch_vccnz .LBB0_1381
	ds_read_b64_tr_b16 v[4:5], v100
	ds_read_b64_tr_b16 v[6:7], v100 offset:2048
	s_nop 5
	ds_read_b64_tr_b16 v[20:21], v100 offset:4096
	ds_read_b64_tr_b16 v[22:23], v100 offset:6144
	s_waitcnt lgkmcnt(2)
	s_setprio 1
	v_mfma_f32_32x32x16_bf16 v[4:19], v[84:87], v[4:7], 0
	s_waitcnt lgkmcnt(0)
	v_mfma_f32_32x32x16_bf16 v[4:19], v[88:91], v[20:23], v[4:19]
	ds_read_b64_tr_b16 v[20:21], v100 offset:8192
	ds_read_b64_tr_b16 v[22:23], v100 offset:10240
	s_waitcnt lgkmcnt(0)
	v_mfma_f32_32x32x16_bf16 v[4:19], v[96:99], v[20:23], v[4:19]
	ds_read_b64_tr_b16 v[20:21], v100 offset:12288
	ds_read_b64_tr_b16 v[22:23], v100 offset:14336
	s_waitcnt lgkmcnt(0)
	v_mfma_f32_32x32x16_bf16 v[4:19], v[92:95], v[20:23], v[4:19]
	ds_read_b64_tr_b16 v[22:23], v100 offset:2560
	ds_read_b64_tr_b16 v[20:21], v100 offset:512
	s_waitcnt lgkmcnt(0)
	v_mfma_f32_32x32x16_bf16 v[20:35], v[84:87], v[20:23], 0
	ds_read_b64_tr_b16 v[86:87], v100 offset:6656
	ds_read_b64_tr_b16 v[84:85], v100 offset:4608
	s_waitcnt lgkmcnt(0)
	v_mfma_f32_32x32x16_bf16 v[20:35], v[88:91], v[84:87], v[20:35]
	ds_read_b64_tr_b16 v[86:87], v100 offset:10752
	ds_read_b64_tr_b16 v[84:85], v100 offset:8704
	s_waitcnt lgkmcnt(0)
	v_mfma_f32_32x32x16_bf16 v[20:35], v[96:99], v[84:87], v[20:35]
	ds_read_b64_tr_b16 v[86:87], v100 offset:14848
	ds_read_b64_tr_b16 v[84:85], v100 offset:12800
	s_waitcnt lgkmcnt(0)
	v_mfma_f32_32x32x16_bf16 v[20:35], v[92:95], v[84:87], v[20:35]
	s_setprio 0
.LBB0_1381:
	s_cmp_lt_u32 s9, 64
	s_cbranch_scc1 .LBB0_1387
	v_or_b32_e32 v84, 64, v183
	v_cmp_le_u32_e32 vcc, v84, v182
	v_or_b32_e32 v84, 0x41, v183
	s_nop 0
	v_cndmask_b32_e32 v64, 0, v64, vcc
	v_cmp_le_u32_e32 vcc, v84, v182
	v_or_b32_e32 v84, 0x42, v183
	s_nop 0
	v_cndmask_b32_e32 v65, 0, v65, vcc
	v_cmp_le_u32_e32 vcc, v84, v182
	v_or_b32_e32 v84, 0x43, v183
	s_nop 0
	v_cndmask_b32_e32 v66, 0, v66, vcc
	v_cmp_le_u32_e32 vcc, v84, v182
	v_or_b32_e32 v84, 0x44, v183
	s_nop 0
	v_cndmask_b32_e32 v67, 0, v67, vcc
	v_cmp_le_u32_e32 vcc, v84, v182
	v_or_b32_e32 v84, 0x45, v183
	v_cvt_pk_bf16_f32 v85, v66, v67
	v_cndmask_b32_e32 v60, 0, v60, vcc
	v_cmp_le_u32_e32 vcc, v84, v182
	v_or_b32_e32 v84, 0x46, v183
	s_nop 0
	v_cndmask_b32_e32 v61, 0, v61, vcc
	v_cmp_le_u32_e32 vcc, v84, v182
	v_or_b32_e32 v84, 0x47, v183
	v_cvt_pk_bf16_f32 v86, v60, v61
	v_cndmask_b32_e32 v62, 0, v62, vcc
	v_cmp_le_u32_e32 vcc, v84, v182
	v_or_b32_e32 v60, 0x50, v183
	v_cvt_pk_bf16_f32 v84, v64, v65
	v_cndmask_b32_e32 v63, 0, v63, vcc
	v_cmp_le_u32_e32 vcc, v60, v182
	v_or_b32_e32 v60, 0x51, v183
	v_cvt_pk_bf16_f32 v87, v62, v63
	v_cndmask_b32_e32 v56, 0, v56, vcc
	v_cmp_le_u32_e32 vcc, v60, v182
	v_or_b32_e32 v60, 0x52, v183
	s_nop 0
	v_cndmask_b32_e32 v57, 0, v57, vcc
	v_cmp_le_u32_e32 vcc, v60, v182
	v_or_b32_e32 v60, 0x53, v183
	v_cvt_pk_bf16_f32 v88, v56, v57
	v_cndmask_b32_e32 v58, 0, v58, vcc
	v_cmp_le_u32_e32 vcc, v60, v182
	v_or_b32_e32 v60, 0x54, v183
	s_nop 0
	v_cndmask_b32_e32 v59, 0, v59, vcc
	v_cmp_le_u32_e32 vcc, v60, v182
	v_or_b32_e32 v60, 0x55, v183
	v_cvt_pk_bf16_f32 v89, v58, v59
	v_cndmask_b32_e32 v52, 0, v52, vcc
	v_cmp_le_u32_e32 vcc, v60, v182
	v_or_b32_e32 v60, 0x56, v183
	s_nop 0
	v_cndmask_b32_e32 v53, 0, v53, vcc
	v_cmp_le_u32_e32 vcc, v60, v182
	v_or_b32_e32 v60, 0x57, v183
	v_cvt_pk_bf16_f32 v90, v52, v53
	v_cndmask_b32_e32 v54, 0, v54, vcc
	v_cmp_le_u32_e32 vcc, v60, v182
	v_or_b32_e32 v52, 0x60, v183
	s_nop 0
	v_cndmask_b32_e32 v55, 0, v55, vcc
	v_cmp_le_u32_e32 vcc, v52, v182
	v_or_b32_e32 v52, 0x61, v183
	v_cvt_pk_bf16_f32 v91, v54, v55
	v_cndmask_b32_e32 v48, 0, v48, vcc
	v_cmp_le_u32_e32 vcc, v52, v182
	v_or_b32_e32 v52, 0x62, v183
	s_nop 0
	v_cndmask_b32_e32 v49, 0, v49, vcc
	v_cmp_le_u32_e32 vcc, v52, v182
	v_or_b32_e32 v52, 0x63, v183
	v_cvt_pk_bf16_f32 v92, v48, v49
	v_cndmask_b32_e32 v50, 0, v50, vcc
	v_cmp_le_u32_e32 vcc, v52, v182
	v_or_b32_e32 v52, 0x64, v183
	s_nop 0
	v_cndmask_b32_e32 v51, 0, v51, vcc
	v_cmp_le_u32_e32 vcc, v52, v182
	v_or_b32_e32 v52, 0x65, v183
	v_cvt_pk_bf16_f32 v93, v50, v51
	v_cndmask_b32_e32 v44, 0, v44, vcc
	v_cmp_le_u32_e32 vcc, v52, v182
	v_or_b32_e32 v52, 0x66, v183
	s_nop 0
	v_cndmask_b32_e32 v45, 0, v45, vcc
	v_cmp_le_u32_e32 vcc, v52, v182
	v_or_b32_e32 v52, 0x67, v183
	v_cvt_pk_bf16_f32 v94, v44, v45
	v_cndmask_b32_e32 v46, 0, v46, vcc
	v_cmp_le_u32_e32 vcc, v52, v182
	v_or_b32_e32 v44, 0x70, v183
	s_nop 0
	v_cndmask_b32_e32 v47, 0, v47, vcc
	v_cmp_le_u32_e32 vcc, v44, v182
	v_or_b32_e32 v44, 0x71, v183
	v_cvt_pk_bf16_f32 v95, v46, v47
	v_cndmask_b32_e32 v40, 0, v40, vcc
	v_cmp_le_u32_e32 vcc, v44, v182
	v_or_b32_e32 v44, 0x72, v183
	s_nop 0
	v_cndmask_b32_e32 v41, 0, v41, vcc
	v_cmp_le_u32_e32 vcc, v44, v182
	v_or_b32_e32 v44, 0x73, v183
	v_cvt_pk_bf16_f32 v96, v40, v41
	v_cndmask_b32_e32 v42, 0, v42, vcc
	v_cmp_le_u32_e32 vcc, v44, v182
	v_or_b32_e32 v44, 0x74, v183
	s_nop 0
	v_cndmask_b32_e32 v43, 0, v43, vcc
	v_cmp_le_u32_e32 vcc, v44, v182
	v_or_b32_e32 v44, 0x75, v183
	v_cvt_pk_bf16_f32 v97, v42, v43
	v_cndmask_b32_e32 v36, 0, v36, vcc
	v_cmp_le_u32_e32 vcc, v44, v182
	v_or_b32_e32 v44, 0x76, v183
	s_nop 0
	v_cndmask_b32_e32 v37, 0, v37, vcc
	v_cmp_le_u32_e32 vcc, v44, v182
	v_or_b32_e32 v44, 0x77, v183
	v_cvt_pk_bf16_f32 v98, v36, v37
	v_cndmask_b32_e32 v38, 0, v38, vcc
	v_cmp_le_u32_e32 vcc, v44, v182
	s_nop 1
	v_cndmask_b32_e32 v39, 0, v39, vcc
	v_cvt_pk_bf16_f32 v99, v38, v39
	s_andn2_b64 vcc, exec, s[0:1]
	s_mov_b64 s[0:1], -1
	s_cbranch_vccnz .LBB0_1384
; #define LAS __attribute__((address_space(3)))
; __device__ __forceinline__ s16x4 tr_read(LAS const unsigned char* p) { return __builtin_bit_cast(s16x4, __builtin_amdgcn_ds_read_tr16_b64_v4i16((LAS v4i16_t*)p)); }
; template <int D0> __device__ __forceinline__ void pv_one(f32x16& od, LAS const unsigned char* vb, bf16x8 pa0, bf16x8 pa1, bf16x8 pa2, bf16x8 pa3) {
;     const s16x4 l0 = tr_read(vb + v_rd_off(D0, 0, 0)), h0 = tr_read(vb + v_rd_off(D0, 0, 1)), l1 = tr_read(vb + v_rd_off(D0, 1, 0)), h1 = tr_read(vb + v_rd_off(D0, 1, 1));
;     const s16x4 l2 = tr_read(vb + v_rd_off(D0, 2, 0)), h2 = tr_read(vb + v_rd_off(D0, 2, 1)), l3 = tr_read(vb + v_rd_off(D0, 3, 0)), h3 = tr_read(vb + v_rd_off(D0, 3, 1));
;     ...
;     od = __builtin_amdgcn_mfma_f32_32x32x16_bf16(pa0, ATT_PK(l0, h0), od, 0, 0, 0);
;     od = __builtin_amdgcn_mfma_f32_32x32x16_bf16(pa1, ATT_PK(l1, h1), od, 0, 0, 0);
;     od = __builtin_amdgcn_mfma_f32_32x32x16_bf16(pa2, ATT_PK(l2, h2), od, 0, 0, 0);
;     od = __builtin_amdgcn_mfma_f32_32x32x16_bf16(pa3, ATT_PK(l3, h3), od, 0, 0, 0);
; __device__ __forceinline__ void unit(const bf16_t* proj, const float* stats  , const float* lng, const float* lnb, const float* sw, const float* sb, bf16_t* Y2, int un, LAS unsigned char* lds) {
;     ...
;         if (eh == 0) { att::pv_one<0>(o0, vb + st * att::SHM_V, pa[0], pa[1], pa[2], pa[3]); att::pv_one<1>(o1, vb + st * att::SHM_V, pa[0], pa[1], pa[2], pa[3]); }
;         else         { att::pv_one<2>(o0, vb + st * att::SHM_V, pa[0], pa[1], pa[2], pa[3]); att::pv_one<3>(o1, vb + st * att::SHM_V, pa[0], pa[1], pa[2], pa[3]); }
	ds_read_b64_tr_b16 v[52:53], v100 offset:17408
	ds_read_b64_tr_b16 v[54:55], v100 offset:19456
	s_mov_b64 s[0:1], 0
	s_waitcnt lgkmcnt(0)
	s_setprio 1
	v_mfma_f32_32x32x16_bf16 v[36:51], v[84:87], v[52:55], v[4:19]
	ds_read_b64_tr_b16 v[52:53], v100 offset:21504
	ds_read_b64_tr_b16 v[54:55], v100 offset:23552
	s_waitcnt lgkmcnt(0)
	v_mfma_f32_32x32x16_bf16 v[36:51], v[88:91], v[52:55], v[36:51]
	ds_read_b64_tr_b16 v[52:53], v100 offset:25600
	ds_read_b64_tr_b16 v[54:55], v100 offset:27648
	s_waitcnt lgkmcnt(0)
	v_mfma_f32_32x32x16_bf16 v[36:51], v[92:95], v[52:55], v[36:51]
	ds_read_b64_tr_b16 v[52:53], v100 offset:29696
	ds_read_b64_tr_b16 v[54:55], v100 offset:31744
	ds_read_b64_tr_b16 v[104:105], v100 offset:19968
	ds_read_b64_tr_b16 v[102:103], v100 offset:17920
	s_waitcnt lgkmcnt(2)
	v_mfma_f32_32x32x16_bf16 v[36:51], v[96:99], v[52:55], v[36:51]
	s_waitcnt lgkmcnt(0)
	v_mfma_f32_32x32x16_bf16 v[52:67], v[84:87], v[102:105], v[20:35]
	ds_read_b64_tr_b16 v[104:105], v100 offset:24064
	ds_read_b64_tr_b16 v[102:103], v100 offset:22016
	s_waitcnt lgkmcnt(0)
	v_mfma_f32_32x32x16_bf16 v[52:67], v[88:91], v[102:105], v[52:67]
	ds_read_b64_tr_b16 v[104:105], v100 offset:28160
	ds_read_b64_tr_b16 v[102:103], v100 offset:26112
	s_waitcnt lgkmcnt(0)
	v_mfma_f32_32x32x16_bf16 v[52:67], v[92:95], v[102:105], v[52:67]
	ds_read_b64_tr_b16 v[104:105], v100 offset:32256
	ds_read_b64_tr_b16 v[102:103], v100 offset:30208
	s_waitcnt lgkmcnt(0)
	v_mfma_f32_32x32x16_bf16 v[52:67], v[96:99], v[102:105], v[52:67]
	s_setprio 0
.LBB0_1384:
	s_andn2_b64 vcc, exec, s[0:1]
	s_cbranch_vccnz .LBB0_1386
	ds_read_b64_tr_b16 v[36:37], v100 offset:16384
	ds_read_b64_tr_b16 v[38:39], v100 offset:18432
	s_waitcnt lgkmcnt(0)
	s_setprio 1
	v_mfma_f32_32x32x16_bf16 v[4:19], v[84:87], v[36:39], v[4:19]
	ds_read_b64_tr_b16 v[36:37], v100 offset:20480
	ds_read_b64_tr_b16 v[38:39], v100 offset:22528
	s_waitcnt lgkmcnt(0)
	v_mfma_f32_32x32x16_bf16 v[4:19], v[88:91], v[36:39], v[4:19]
	ds_read_b64_tr_b16 v[36:37], v100 offset:24576
	ds_read_b64_tr_b16 v[38:39], v100 offset:26624
	s_waitcnt lgkmcnt(0)
	v_mfma_f32_32x32x16_bf16 v[4:19], v[92:95], v[36:39], v[4:19]
	ds_read_b64_tr_b16 v[38:39], v100 offset:18944
	ds_read_b64_tr_b16 v[36:37], v100 offset:16896
	s_waitcnt lgkmcnt(0)
	v_mfma_f32_32x32x16_bf16 v[20:35], v[84:87], v[36:39], v[20:35]
	ds_read_b64_tr_b16 v[38:39], v100 offset:23040
	ds_read_b64_tr_b16 v[36:37], v100 offset:20992
	s_waitcnt lgkmcnt(0)
	v_mfma_f32_32x32x16_bf16 v[20:35], v[88:91], v[36:39], v[20:35]
	ds_read_b64_tr_b16 v[38:39], v100 offset:27136
	ds_read_b64_tr_b16 v[36:37], v100 offset:25088
	s_waitcnt lgkmcnt(0)
	v_mfma_f32_32x32x16_bf16 v[20:35], v[92:95], v[36:39], v[20:35]
	ds_read_b64_tr_b16 v[38:39], v100 offset:31232
	ds_read_b64_tr_b16 v[36:37], v100 offset:29184
	s_waitcnt lgkmcnt(0)
	v_mfma_f32_32x32x16_bf16 v[20:35], v[96:99], v[36:39], v[20:35]
	ds_read_b64_tr_b16 v[38:39], v100 offset:30720
	ds_read_b64_tr_b16 v[36:37], v100 offset:28672
	s_waitcnt lgkmcnt(0)
	v_mfma_f32_32x32x16_bf16 v[4:19], v[96:99], v[36:39], v[4:19]
	s_nop 7
	v_mov_b64_e32 v[66:67], v[34:35]
	v_mov_b64_e32 v[64:65], v[32:33]
	v_mov_b64_e32 v[62:63], v[30:31]
	v_mov_b64_e32 v[60:61], v[28:29]
	v_mov_b64_e32 v[58:59], v[26:27]
	v_mov_b64_e32 v[56:57], v[24:25]
	v_mov_b64_e32 v[54:55], v[22:23]
	v_mov_b64_e32 v[50:51], v[18:19]
	v_mov_b64_e32 v[52:53], v[20:21]
	v_mov_b64_e32 v[48:49], v[16:17]
	v_mov_b64_e32 v[46:47], v[14:15]
	v_mov_b64_e32 v[44:45], v[12:13]
	v_mov_b64_e32 v[42:43], v[10:11]
	v_mov_b64_e32 v[40:41], v[8:9]
	v_mov_b64_e32 v[38:39], v[6:7]
	v_mov_b64_e32 v[36:37], v[4:5]
	s_setprio 0
